# topk-phase weight-conversion window split across all workgroups (3 items per wave on WGs>=128, 2 on WGs<128)
# baseline (speedup 1.0000x reference)
.LBB0_1347:
	v_readlane_b32 s4, v254, 61
	s_cmpk_gt_i32 s4, 0x7f
	v_readlane_b32 s2, v254, 39
	s_cselect_b64 s[0:1], -1, 0
	v_readlane_b32 s3, v254, 40
	s_mov_b64 s[0:1], s[2:3]
	s_andn2_b64 vcc, exec, s[0:1]
	s_mov_b32 s29, 0xffff0000
	s_movk_i32 s33, 0x7fff
	v_readlane_b32 s56, v255, 7
	s_cbranch_vccnz .LBB0_1361
	v_readlane_b32 s0, v255, 1
	v_readlane_b32 s1, v255, 2
	s_and_b64 s[0:1], s[0:1], exec
	s_movk_i32 s0, 0xe00
	v_readlane_b32 s1, v254, 59
	s_cselect_b32 s2, s0, 0x600
	s_cmp_eq_u32 s1, 0
	s_mov_b32 s0, 0x9000
	s_cselect_b32 s0, 0x1800, s0
	s_cmp_gt_u32 s1, 1
	s_cselect_b32 s1, 0x7000, 0
	v_readlane_b32 s6, v255, 3
	s_add_i32 s3, s0, s1
	v_readlane_b32 s7, v255, 4
	s_and_b64 s[0:1], s[6:7], exec
	s_cselect_b32 s0, 0x7800, 0
	s_add_i32 s3, s3, s0
	s_and_b64 s[0:1], s[6:7], exec
	s_cselect_b32 s0, 0, 0x1c00
	s_add_i32 s0, s3, s0
	s_add_i32 s2, s0, s2
	s_cmpk_gt_i32 s4, 0x7f
	s_cselect_b32 s100, 2, 1
	s_cselect_b32 s3, 24, 16
	s_movk_i32 s101, 0xc00
	s_cselect_b32 s101, 0xfffff400, s101
	s_mul_i32 s3, s4, s3
	s_add_i32 s3, s3, s101
	v_readlane_b32 s4, v253, 8
	s_add_i32 s4, s2, s56
	s_add_i32 s12, s4, s3
	s_min_u32 s14, s2, 0x16c00
	v_readlane_b32 s10, v253, 14
	v_readlane_b32 s11, v253, 15
	s_nop 0
	s_addk_i32 s14, 0x1400
	s_mov_b64 s[0:1], s[10:11]
	s_cmp_ge_i32 s12, s14
	v_readlane_b32 s5, v253, 9
	v_readlane_b32 s6, v253, 10
	v_readlane_b32 s7, v253, 11
	v_readlane_b32 s8, v253, 12
	v_readlane_b32 s9, v253, 13
	v_mbcnt_lo_u32_b32 v0, -1, 0
	v_mbcnt_hi_u32_b32 v0, -1, v0
	s_cbranch_scc1 .LBB0_1361
	s_mul_hi_i32 s2, s12, 0x2aaaaaab
	s_lshr_b32 s3, s2, 31
	s_ashr_i32 s2, s2, 12
	s_add_i32 s3, s2, s3
	s_mul_i32 s2, s3, 0x6000
	s_sub_i32 s17, s12, s2
	s_lshl_b32 s13, s17, 5
	s_lshl_b32 s3, s3, 4
	s_bfe_u32 s4, s17, 0x40009
	s_bfe_u32 s16, s17, 0x40005
	s_and_b32 s2, s13, 0x3e0
	s_ashr_i32 s15, s17, 13
	s_or_b32 s8, s4, s3
	s_cmp_gt_i32 s15, 1
	s_mov_b64 s[10:11], -1
	s_cbranch_scc0 .LBB0_1351
	s_ashr_i32 s9, s8, 31
	v_readlane_b32 s20, v253, 8
	s_lshl_b64 s[4:5], s[8:9], 22
	v_readlane_b32 s22, v253, 10
	v_readlane_b32 s23, v253, 11
	s_add_u32 s3, s22, s4
	s_addc_u32 s4, s23, s5
	s_lshl_b32 s30, s16, 6
	s_lshl_b32 s5, s16, 18
	s_add_u32 s5, s3, s5
	s_addc_u32 s4, s4, 0
	s_lshl_b32 s6, s2, 2
	s_add_u32 s6, s5, s6
	s_addc_u32 s7, s4, 0
	s_lshl_b64 s[4:5], s[8:9], 21
	s_add_u32 s4, s0, s4
	s_addc_u32 s5, s1, s5
	s_add_u32 s4, s4, 0x31a00000
	v_readlane_b32 s21, v253, 9
	v_readlane_b32 s24, v253, 12
	v_readlane_b32 s25, v253, 13
	v_readlane_b32 s26, v253, 14
	v_readlane_b32 s27, v253, 15
	s_mov_b32 s3, s31
	s_addc_u32 s5, s5, 0
	s_mov_b64 s[10:11], 0

.LBB0_1356:
	s_cmp_ge_u32 s15, s100
	s_cselect_b64 s[0:1], -1, 0
	s_cmp_ge_i32 s20, s14
	s_cselect_b64 s[6:7], -1, 0
	s_or_b64 s[0:1], s[0:1], s[6:7]
	s_and_b64 vcc, exec, s[0:1]
	s_cbranch_vccnz .LBB0_1355
	s_mul_hi_i32 s2, s20, 0x2aaaaaab
	s_lshr_b32 s3, s2, 31
	s_ashr_i32 s2, s2, 12
	s_add_i32 s3, s2, s3
	s_mul_i32 s2, s3, 0xffffa000
	s_add_i32 s25, s20, s2
	s_mul_i32 s2, s3, 0xfff40000
	s_add_i32 s22, s21, s2
	s_lshl_b32 s3, s3, 4
	s_bfe_u32 s6, s25, 0x40009
	s_bfe_u32 s24, s25, 0x40005
	s_and_b32 s2, s22, 0x3e0
	s_ashr_i32 s23, s25, 13
	s_or_b32 s10, s6, s3
	s_cmp_gt_i32 s23, 1
	s_mov_b64 s[12:13], -1
	s_cbranch_scc0 .LBB0_1359
	s_ashr_i32 s11, s10, 31
	v_readlane_b32 s36, v253, 8
	s_lshl_b64 s[6:7], s[10:11], 22
	v_readlane_b32 s38, v253, 10
	v_readlane_b32 s39, v253, 11
	s_add_u32 s3, s38, s6
	s_addc_u32 s6, s39, s7
	s_lshl_b32 s30, s24, 6
	s_lshl_b32 s7, s24, 18
	s_add_u32 s7, s3, s7
	s_addc_u32 s6, s6, 0
	s_lshl_b32 s8, s2, 2
	s_add_u32 s8, s7, s8
	s_addc_u32 s9, s6, 0
	s_lshl_b64 s[6:7], s[10:11], 21
	s_add_u32 s6, s16, s6
	v_readlane_b32 s37, v253, 9
	v_readlane_b32 s40, v253, 12
	v_readlane_b32 s41, v253, 13
	v_readlane_b32 s42, v253, 14
	v_readlane_b32 s43, v253, 15
	s_mov_b32 s3, s31
	s_addc_u32 s7, s17, s7
	s_mov_b64 s[12:13], 0

	.amdhsa_kernel _ZN12_GLOBAL__N_18mega_fwdENS_1PE
		.amdhsa_group_segment_fixed_size 0
		.amdhsa_private_segment_fixed_size 0
		.amdhsa_kernarg_size 496
		.amdhsa_user_sgpr_count 2
		.amdhsa_user_sgpr_dispatch_ptr 0
		.amdhsa_user_sgpr_queue_ptr 0
		.amdhsa_user_sgpr_kernarg_segment_ptr 1
		.amdhsa_user_sgpr_dispatch_id 0
		.amdhsa_user_sgpr_kernarg_preload_length 0
		.amdhsa_user_sgpr_kernarg_preload_offset 0
		.amdhsa_user_sgpr_private_segment_size 0
		.amdhsa_uses_dynamic_stack 0
		.amdhsa_enable_private_segment 0
		.amdhsa_system_sgpr_workgroup_id_x 1
		.amdhsa_system_sgpr_workgroup_id_y 0
		.amdhsa_system_sgpr_workgroup_id_z 0
		.amdhsa_system_sgpr_workgroup_info 0
		.amdhsa_system_vgpr_workitem_id 0
		.amdhsa_next_free_vgpr 256
		.amdhsa_next_free_sgpr 102
		.amdhsa_accum_offset 256
		.amdhsa_reserve_vcc 1
		.amdhsa_float_round_mode_32 0
		.amdhsa_float_round_mode_16_64 0
		.amdhsa_float_denorm_mode_32 3
		.amdhsa_float_denorm_mode_16_64 3
		.amdhsa_dx10_clamp 1
		.amdhsa_ieee_mode 1
		.amdhsa_fp16_overflow 0
		.amdhsa_tg_split 0
		.amdhsa_exception_fp_ieee_invalid_op 0
		.amdhsa_exception_fp_denorm_src 0
		.amdhsa_exception_fp_ieee_div_zero 0
		.amdhsa_exception_fp_ieee_overflow 0
		.amdhsa_exception_fp_ieee_underflow 0
		.amdhsa_exception_fp_ieee_inexact 0
		.amdhsa_exception_int_div_zero 0
	.end_amdhsa_kernel

amdhsa.kernels:
  - .agpr_count:     0
    .args:
      - .offset:         0
        .size:           240
        .value_kind:     by_value
      - .offset:         240
        .size:           4
        .value_kind:     hidden_block_count_x
      - .offset:         244
        .size:           4
        .value_kind:     hidden_block_count_y
      - .offset:         248
        .size:           4
        .value_kind:     hidden_block_count_z
      - .offset:         252
        .size:           2
        .value_kind:     hidden_group_size_x
      - .offset:         254
        .size:           2
        .value_kind:     hidden_group_size_y
      - .offset:         256
        .size:           2
        .value_kind:     hidden_group_size_z
      - .offset:         258
        .size:           2
        .value_kind:     hidden_remainder_x
      - .offset:         260
        .size:           2
        .value_kind:     hidden_remainder_y
      - .offset:         262
        .size:           2
        .value_kind:     hidden_remainder_z
      - .offset:         280
        .size:           8
        .value_kind:     hidden_global_offset_x
      - .offset:         288
        .size:           8
        .value_kind:     hidden_global_offset_y
      - .offset:         296
        .size:           8
        .value_kind:     hidden_global_offset_z
      - .offset:         304
        .size:           2
        .value_kind:     hidden_grid_dims
      - .offset:         360
        .size:           4
        .value_kind:     hidden_dynamic_lds_size
    .group_segment_fixed_size: 0
    .kernarg_segment_align: 8
    .kernarg_segment_size: 496
    .language:       OpenCL C
    .language_version:
      - 2
      - 0
    .max_flat_workgroup_size: 512
    .name:           _ZN12_GLOBAL__N_18mega_fwdENS_1PE
    .private_segment_fixed_size: 0
    .sgpr_count:     108
    .sgpr_spill_count: 200
    .symbol:         _ZN12_GLOBAL__N_18mega_fwdENS_1PE.kd
    .uniform_work_group_size: 1
    .uses_dynamic_stack: false
    .vgpr_count:     256
    .vgpr_spill_count: 0
    .wavefront_size: 64
